# k_fold2 tail: bias loads + kernarg loads hoisted before the reduction, DPP reduction instead of 6 ds_bpermute round trips
# baseline (speedup 1.0000x reference)
.LBB3_22:
	s_load_dwordx4 s[32:35], s[0:1], 0x38
	s_load_dwordx2 s[36:37], s[0:1], 0x50
	v_lshlrev_b32_e32 v0, 2, v1
	ds_read2st64_b32 v[4:5], v0 offset0:4 offset1:5
	ds_read2st64_b32 v[6:7], v0 offset0:6 offset1:7
	v_lshlrev_b32_e32 v8, 2, v2
	s_waitcnt lgkmcnt(0)
	global_load_dword v9, v8, s[32:33]
	global_load_dword v10, v8, s[34:35]
	v_fma_f32 v4, v14, v4, 0
	v_fmac_f32_e32 v4, v19, v5
	v_fmac_f32_e32 v4, v18, v6
	v_fmac_f32_e32 v4, v20, v7
	s_nop 1
	v_add_f32_dpp v4, v4, v4 row_shr:1 row_mask:0xf bank_mask:0xf bound_ctrl:0
	s_nop 1
	v_add_f32_dpp v4, v4, v4 row_shr:2 row_mask:0xf bank_mask:0xf bound_ctrl:0
	s_nop 1
	v_add_f32_dpp v4, v4, v4 row_shr:4 row_mask:0xf bank_mask:0xf bound_ctrl:0
	s_nop 1
	v_add_f32_dpp v4, v4, v4 row_shr:8 row_mask:0xf bank_mask:0xf bound_ctrl:0
	s_nop 1
	v_add_f32_dpp v4, v4, v4 row_bcast:15 row_mask:0xa bank_mask:0xf
	s_nop 1
	v_add_f32_dpp v4, v4, v4 row_bcast:31 row_mask:0xc bank_mask:0xf
	v_cmp_eq_u32_e32 vcc, 63, v1
	s_and_b64 exec, exec, vcc
	s_cbranch_execz .LBB3_18
	v_and_b32_e32 v3, 0xffffff80, v2
	s_movk_i32 s2, 0x100
	v_mov_b32_e32 v5, 0xbfb8aa3b
	v_mov_b32_e32 v6, 0x4038aa3b
	v_cmp_eq_u32_e32 vcc, s2, v3
	s_waitcnt vmcnt(0)
	v_add_f32_e32 v9, v9, v10
	v_cndmask_b32_e32 v5, v5, v6, vcc
	v_add_f32_e32 v0, v4, v9
	v_mul_f32_e32 v0, v5, v0
	global_store_dword v8, v0, s[36:37]
	s_endpgm

	.amdhsa_kernel _Z7k_fold2PKfS0_S0_S0_S0_S0_S0_S0_S0_PDF16_Pf
		.amdhsa_group_segment_fixed_size 2048
		.amdhsa_private_segment_fixed_size 0
		.amdhsa_kernarg_size 344
		.amdhsa_user_sgpr_count 2
		.amdhsa_user_sgpr_dispatch_ptr 0
		.amdhsa_user_sgpr_queue_ptr 0
		.amdhsa_user_sgpr_kernarg_segment_ptr 1
		.amdhsa_user_sgpr_dispatch_id 0
		.amdhsa_user_sgpr_kernarg_preload_length 0
		.amdhsa_user_sgpr_kernarg_preload_offset 0
		.amdhsa_user_sgpr_private_segment_size 0
		.amdhsa_uses_dynamic_stack 0
		.amdhsa_enable_private_segment 0
		.amdhsa_system_sgpr_workgroup_id_x 1
		.amdhsa_system_sgpr_workgroup_id_y 0
		.amdhsa_system_sgpr_workgroup_id_z 0
		.amdhsa_system_sgpr_workgroup_info 0
		.amdhsa_system_vgpr_workitem_id 0
		.amdhsa_next_free_vgpr 61
		.amdhsa_next_free_sgpr 38
		.amdhsa_accum_offset 64
		.amdhsa_reserve_vcc 1
		.amdhsa_float_round_mode_32 0
		.amdhsa_float_round_mode_16_64 0
		.amdhsa_float_denorm_mode_32 3
		.amdhsa_float_denorm_mode_16_64 3
		.amdhsa_dx10_clamp 1
		.amdhsa_ieee_mode 1
		.amdhsa_fp16_overflow 0
		.amdhsa_tg_split 0
		.amdhsa_exception_fp_ieee_invalid_op 0
		.amdhsa_exception_fp_denorm_src 0
		.amdhsa_exception_fp_ieee_div_zero 0
		.amdhsa_exception_fp_ieee_overflow 0
		.amdhsa_exception_fp_ieee_underflow 0
		.amdhsa_exception_fp_ieee_inexact 0
		.amdhsa_exception_int_div_zero 0
	.end_amdhsa_kernel

amdhsa.kernels:
  - .agpr_count:     0
    .args:
      - .actual_access:  read_only
        .address_space:  global
        .offset:         0
        .size:           8
        .value_kind:     global_buffer
      - .actual_access:  read_only
        .address_space:  global
        .offset:         8
        .size:           8
        .value_kind:     global_buffer
      - .actual_access:  read_only
        .address_space:  global
        .offset:         16
        .size:           8
        .value_kind:     global_buffer
      - .actual_access:  read_only
        .address_space:  global
        .offset:         24
        .size:           8
        .value_kind:     global_buffer
      - .actual_access:  write_only
        .address_space:  global
        .offset:         32
        .size:           8
        .value_kind:     global_buffer
      - .actual_access:  write_only
        .address_space:  global
        .offset:         40
        .size:           8
        .value_kind:     global_buffer
    .group_segment_fixed_size: 56512
    .kernarg_segment_align: 8
    .kernarg_segment_size: 48
    .language:       OpenCL C
    .language_version:
      - 2
      - 0
    .max_flat_workgroup_size: 1024
    .name:           _Z10k_bscatterPKiS0_PKfS0_PiP15HIP_vector_typeIiLj2EE
    .private_segment_fixed_size: 0
    .sgpr_count:     42
    .sgpr_spill_count: 0
    .symbol:         _Z10k_bscatterPKiS0_PKfS0_PiP15HIP_vector_typeIiLj2EE.kd
    .uniform_work_group_size: 1
    .uses_dynamic_stack: false
    .vgpr_count:     89
    .vgpr_spill_count: 0
    .wavefront_size: 64
  - .agpr_count:     0
    .args:
      - .actual_access:  read_only
        .address_space:  global
        .offset:         0
        .size:           8
        .value_kind:     global_buffer
      - .actual_access:  read_only
        .address_space:  global
        .offset:         8
        .size:           8
        .value_kind:     global_buffer
      - .actual_access:  write_only
        .address_space:  global
        .offset:         16
        .size:           8
        .value_kind:     global_buffer
      - .actual_access:  write_only
        .address_space:  global
        .offset:         24
        .size:           8
        .value_kind:     global_buffer
      - .actual_access:  write_only
        .address_space:  global
        .offset:         32
        .size:           8
        .value_kind:     global_buffer
      - .actual_access:  write_only
        .address_space:  global
        .offset:         40
        .size:           8
        .value_kind:     global_buffer
      - .actual_access:  read_only
        .address_space:  global
        .offset:         48
        .size:           8
        .value_kind:     global_buffer
      - .actual_access:  write_only
        .address_space:  global
        .offset:         56
        .size:           8
        .value_kind:     global_buffer
    .group_segment_fixed_size: 12352
    .kernarg_segment_align: 8
    .kernarg_segment_size: 64
    .language:       OpenCL C
    .language_version:
      - 2
      - 0
    .max_flat_workgroup_size: 1024
    .name:           _Z8k_bfinalPK15HIP_vector_typeIiLj2EEPKiPS0_PiS6_PfPKfPDF16_
    .private_segment_fixed_size: 0
    .sgpr_count:     38
    .sgpr_spill_count: 0
    .symbol:         _Z8k_bfinalPK15HIP_vector_typeIiLj2EEPKiPS0_PiS6_PfPKfPDF16_.kd
    .uniform_work_group_size: 1
    .uses_dynamic_stack: false
    .vgpr_count:     72
    .vgpr_spill_count: 0
    .wavefront_size: 64
  - .agpr_count:     0
    .args:
      - .actual_access:  read_only
        .address_space:  global
        .offset:         0
        .size:           8
        .value_kind:     global_buffer
      - .actual_access:  write_only
        .address_space:  global
        .offset:         8
        .size:           8
        .value_kind:     global_buffer
      - .actual_access:  write_only
        .address_space:  global
        .offset:         16
        .size:           8
        .value_kind:     global_buffer
      - .actual_access:  read_only
        .address_space:  global
        .offset:         24
        .size:           8
        .value_kind:     global_buffer
      - .actual_access:  read_only
        .address_space:  global
        .offset:         32
        .size:           8
        .value_kind:     global_buffer
      - .actual_access:  write_only
        .address_space:  global
        .offset:         40
        .size:           8
        .value_kind:     global_buffer
      - .actual_access:  read_only
        .address_space:  global
        .offset:         48
        .size:           8
        .value_kind:     global_buffer
      - .actual_access:  read_only
        .address_space:  global
        .offset:         56
        .size:           8
        .value_kind:     global_buffer
      - .actual_access:  read_only
        .address_space:  global
        .offset:         64
        .size:           8
        .value_kind:     global_buffer
      - .actual_access:  read_only
        .address_space:  global
        .offset:         72
        .size:           8
        .value_kind:     global_buffer
      - .actual_access:  read_only
        .address_space:  global
        .offset:         80
        .size:           8
        .value_kind:     global_buffer
      - .actual_access:  read_only
        .address_space:  global
        .offset:         88
        .size:           8
        .value_kind:     global_buffer
      - .actual_access:  write_only
        .address_space:  global
        .offset:         96
        .size:           8
        .value_kind:     global_buffer
      - .actual_access:  write_only
        .address_space:  global
        .offset:         104
        .size:           8
        .value_kind:     global_buffer
      - .actual_access:  write_only
        .address_space:  global
        .offset:         112
        .size:           8
        .value_kind:     global_buffer
      - .actual_access:  write_only
        .address_space:  global
        .offset:         120
        .size:           8
        .value_kind:     global_buffer
      - .actual_access:  write_only
        .address_space:  global
        .offset:         128
        .size:           8
        .value_kind:     global_buffer
    .group_segment_fixed_size: 628
    .kernarg_segment_align: 8
    .kernarg_segment_size: 136
    .language:       OpenCL C
    .language_version:
      - 2
      - 0
    .max_flat_workgroup_size: 1024
    .name:           _Z7k_bhistPKiPiPfPKfS4_PDF16_S4_S4_S4_S4_S4_S4_S5_S5_S5_S5_S2_
    .private_segment_fixed_size: 0
    .sgpr_count:     25
    .sgpr_spill_count: 0
    .symbol:         _Z7k_bhistPKiPiPfPKfS4_PDF16_S4_S4_S4_S4_S4_S4_S5_S5_S5_S5_S2_.kd
    .uniform_work_group_size: 1
    .uses_dynamic_stack: false
    .vgpr_count:     32
    .vgpr_spill_count: 0
    .wavefront_size: 64
  - .agpr_count:     0
    .args:
      - .actual_access:  read_only
        .address_space:  global
        .offset:         0
        .size:           8
        .value_kind:     global_buffer
      - .actual_access:  read_only
        .address_space:  global
        .offset:         8
        .size:           8
        .value_kind:     global_buffer
      - .actual_access:  read_only
        .address_space:  global
        .offset:         16
        .size:           8
        .value_kind:     global_buffer
      - .actual_access:  read_only
        .address_space:  global
        .offset:         24
        .size:           8
        .value_kind:     global_buffer
      - .actual_access:  read_only
        .address_space:  global
        .offset:         32
        .size:           8
        .value_kind:     global_buffer
      - .actual_access:  read_only
        .address_space:  global
        .offset:         40
        .size:           8
        .value_kind:     global_buffer
      - .actual_access:  read_only
        .address_space:  global
        .offset:         48
        .size:           8
        .value_kind:     global_buffer
      - .actual_access:  read_only
        .address_space:  global
        .offset:         56
        .size:           8
        .value_kind:     global_buffer
      - .actual_access:  read_only
        .address_space:  global
        .offset:         64
        .size:           8
        .value_kind:     global_buffer
      - .actual_access:  write_only
        .address_space:  global
        .offset:         72
        .size:           8
        .value_kind:     global_buffer
      - .actual_access:  write_only
        .address_space:  global
        .offset:         80
        .size:           8
        .value_kind:     global_buffer
      - .offset:         88
        .size:           4
        .value_kind:     hidden_block_count_x
      - .offset:         92
        .size:           4
        .value_kind:     hidden_block_count_y
      - .offset:         96
        .size:           4
        .value_kind:     hidden_block_count_z
      - .offset:         100
        .size:           2
        .value_kind:     hidden_group_size_x
      - .offset:         102
        .size:           2
        .value_kind:     hidden_group_size_y
      - .offset:         104
        .size:           2
        .value_kind:     hidden_group_size_z
      - .offset:         106
        .size:           2
        .value_kind:     hidden_remainder_x
      - .offset:         108
        .size:           2
        .value_kind:     hidden_remainder_y
      - .offset:         110
        .size:           2
        .value_kind:     hidden_remainder_z
      - .offset:         128
        .size:           8
        .value_kind:     hidden_global_offset_x
      - .offset:         136
        .size:           8
        .value_kind:     hidden_global_offset_y
      - .offset:         144
        .size:           8
        .value_kind:     hidden_global_offset_z
      - .offset:         152
        .size:           2
        .value_kind:     hidden_grid_dims
    .group_segment_fixed_size: 2048
    .kernarg_segment_align: 8
    .kernarg_segment_size: 344
    .language:       OpenCL C
    .language_version:
      - 2
      - 0
    .max_flat_workgroup_size: 256
    .name:           _Z7k_fold2PKfS0_S0_S0_S0_S0_S0_S0_S0_PDF16_Pf
    .private_segment_fixed_size: 0
    .sgpr_count:     44
    .sgpr_spill_count: 0
    .symbol:         _Z7k_fold2PKfS0_S0_S0_S0_S0_S0_S0_S0_PDF16_Pf.kd
    .uniform_work_group_size: 1
    .uses_dynamic_stack: false
    .vgpr_count:     61
    .vgpr_spill_count: 0
    .wavefront_size: 64
  - .agpr_count:     0
    .args:
      - .actual_access:  read_only
        .address_space:  global
        .offset:         0
        .size:           8
        .value_kind:     global_buffer
      - .actual_access:  read_only
        .address_space:  global
        .offset:         8
        .size:           8
        .value_kind:     global_buffer
      - .actual_access:  write_only
        .address_space:  global
        .offset:         16
        .size:           8
        .value_kind:     global_buffer
      - .actual_access:  read_only
        .address_space:  global
        .offset:         24
        .size:           8
        .value_kind:     global_buffer
      - .actual_access:  read_only
        .address_space:  global
        .offset:         32
        .size:           8
        .value_kind:     global_buffer
      - .actual_access:  read_only
        .address_space:  global
        .offset:         40
        .size:           8
        .value_kind:     global_buffer
      - .actual_access:  read_only
        .address_space:  global
        .offset:         48
        .size:           8
        .value_kind:     global_buffer
      - .actual_access:  read_only
        .address_space:  global
        .offset:         56
        .size:           8
        .value_kind:     global_buffer
      - .actual_access:  read_only
        .address_space:  global
        .offset:         64
        .size:           8
        .value_kind:     global_buffer
      - .actual_access:  read_only
        .address_space:  global
        .offset:         72
        .size:           8
        .value_kind:     global_buffer
      - .actual_access:  read_only
        .address_space:  global
        .offset:         80
        .size:           8
        .value_kind:     global_buffer
      - .actual_access:  write_only
        .address_space:  global
        .offset:         88
        .size:           8
        .value_kind:     global_buffer
      - .actual_access:  write_only
        .address_space:  global
        .offset:         96
        .size:           8
        .value_kind:     global_buffer
      - .address_space:  global
        .offset:         104
        .size:           8
        .value_kind:     global_buffer
      - .actual_access:  write_only
        .address_space:  global
        .offset:         112
        .size:           8
        .value_kind:     global_buffer
      - .actual_access:  read_only
        .address_space:  global
        .offset:         120
        .size:           8
        .value_kind:     global_buffer
      - .actual_access:  read_only
        .address_space:  global
        .offset:         128
        .size:           8
        .value_kind:     global_buffer
    .group_segment_fixed_size: 22272
    .kernarg_segment_align: 8
    .kernarg_segment_size: 136
    .language:       OpenCL C
    .language_version:
      - 2
      - 0
    .max_flat_workgroup_size: 256
    .name:           _Z5k_gcnILi1EEvPKvPK15HIP_vector_typeIiLj2EEPfPKiS8_PKfPKDF16_SA_SA_SA_SA_S6_PDF16_S6_SD_SC_SA_
    .private_segment_fixed_size: 0
    .sgpr_count:     35
    .sgpr_spill_count: 0
    .symbol:         _Z5k_gcnILi1EEvPKvPK15HIP_vector_typeIiLj2EEPfPKiS8_PKfPKDF16_SA_SA_SA_SA_S6_PDF16_S6_SD_SC_SA_.kd
    .uniform_work_group_size: 1
    .uses_dynamic_stack: false
    .vgpr_count:     72
    .vgpr_spill_count: 0
    .wavefront_size: 64
  - .agpr_count:     0
    .args:
      - .actual_access:  read_only
        .address_space:  global
        .offset:         0
        .size:           8
        .value_kind:     global_buffer
      - .actual_access:  read_only
        .address_space:  global
        .offset:         8
        .size:           8
        .value_kind:     global_buffer
      - .actual_access:  read_only
        .address_space:  global
        .offset:         16
        .size:           8
        .value_kind:     global_buffer
      - .actual_access:  read_only
        .address_space:  global
        .offset:         24
        .size:           8
        .value_kind:     global_buffer
      - .actual_access:  read_only
        .address_space:  global
        .offset:         32
        .size:           8
        .value_kind:     global_buffer
      - .actual_access:  read_only
        .address_space:  global
        .offset:         40
        .size:           8
        .value_kind:     global_buffer
      - .actual_access:  read_only
        .address_space:  global
        .offset:         48
        .size:           8
        .value_kind:     global_buffer
      - .actual_access:  read_only
        .address_space:  global
        .offset:         56
        .size:           8
        .value_kind:     global_buffer
      - .actual_access:  read_only
        .address_space:  global
        .offset:         64
        .size:           8
        .value_kind:     global_buffer
      - .actual_access:  read_only
        .address_space:  global
        .offset:         72
        .size:           8
        .value_kind:     global_buffer
      - .actual_access:  read_only
        .address_space:  global
        .offset:         80
        .size:           8
        .value_kind:     global_buffer
      - .actual_access:  read_only
        .address_space:  global
        .offset:         88
        .size:           8
        .value_kind:     global_buffer
      - .actual_access:  write_only
        .address_space:  global
        .offset:         96
        .size:           8
        .value_kind:     global_buffer
      - .address_space:  global
        .offset:         104
        .size:           8
        .value_kind:     global_buffer
      - .actual_access:  read_only
        .address_space:  global
        .offset:         112
        .size:           8
        .value_kind:     global_buffer
      - .actual_access:  read_only
        .address_space:  global
        .offset:         120
        .size:           8
        .value_kind:     global_buffer
      - .actual_access:  read_only
        .address_space:  global
        .offset:         128
        .size:           8
        .value_kind:     global_buffer
      - .offset:         136
        .size:           4
        .value_kind:     hidden_block_count_x
      - .offset:         140
        .size:           4
        .value_kind:     hidden_block_count_y
      - .offset:         144
        .size:           4
        .value_kind:     hidden_block_count_z
      - .offset:         148
        .size:           2
        .value_kind:     hidden_group_size_x
      - .offset:         150
        .size:           2
        .value_kind:     hidden_group_size_y
      - .offset:         152
        .size:           2
        .value_kind:     hidden_group_size_z
      - .offset:         154
        .size:           2
        .value_kind:     hidden_remainder_x
      - .offset:         156
        .size:           2
        .value_kind:     hidden_remainder_y
      - .offset:         158
        .size:           2
        .value_kind:     hidden_remainder_z
      - .offset:         176
        .size:           8
        .value_kind:     hidden_global_offset_x
      - .offset:         184
        .size:           8
        .value_kind:     hidden_global_offset_y
      - .offset:         192
        .size:           8
        .value_kind:     hidden_global_offset_z
      - .offset:         200
        .size:           2
        .value_kind:     hidden_grid_dims
    .group_segment_fixed_size: 32000
    .kernarg_segment_align: 8
    .kernarg_segment_size: 392
    .language:       OpenCL C
    .language_version:
      - 2
      - 0
    .max_flat_workgroup_size: 256
    .name:           _Z5k_gcnILi2EEvPKvPK15HIP_vector_typeIiLj2EEPfPKiS8_PKfPKDF16_SA_SA_SA_SA_S6_PDF16_S6_SD_SC_SA_
    .private_segment_fixed_size: 0
    .sgpr_count:     36
    .sgpr_spill_count: 0
    .symbol:         _Z5k_gcnILi2EEvPKvPK15HIP_vector_typeIiLj2EEPfPKiS8_PKfPKDF16_SA_SA_SA_SA_S6_PDF16_S6_SD_SC_SA_.kd
    .uniform_work_group_size: 1
    .uses_dynamic_stack: false
    .vgpr_count:     128
    .vgpr_spill_count: 0
    .wavefront_size: 64
  - .agpr_count:     0
    .args:
      - .actual_access:  read_only
        .address_space:  global
        .offset:         0
        .size:           8
        .value_kind:     global_buffer
      - .actual_access:  read_only
        .address_space:  global
        .offset:         8
        .size:           8
        .value_kind:     global_buffer
      - .actual_access:  read_only
        .address_space:  global
        .offset:         16
        .size:           8
        .value_kind:     global_buffer
      - .actual_access:  read_only
        .address_space:  global
        .offset:         24
        .size:           8
        .value_kind:     global_buffer
      - .actual_access:  write_only
        .address_space:  global
        .offset:         32
        .size:           8
        .value_kind:     global_buffer
      - .actual_access:  read_only
        .address_space:  global
        .offset:         40
        .size:           8
        .value_kind:     global_buffer
      - .actual_access:  read_only
        .address_space:  global
        .offset:         48
        .size:           8
        .value_kind:     global_buffer
      - .actual_access:  read_only
        .address_space:  global
        .offset:         56
        .size:           8
        .value_kind:     global_buffer
      - .actual_access:  read_only
        .address_space:  global
        .offset:         64
        .size:           8
        .value_kind:     global_buffer
      - .actual_access:  read_only
        .address_space:  global
        .offset:         72
        .size:           8
        .value_kind:     global_buffer
      - .actual_access:  read_only
        .address_space:  global
        .offset:         80
        .size:           8
        .value_kind:     global_buffer
      - .actual_access:  read_only
        .address_space:  global
        .offset:         88
        .size:           8
        .value_kind:     global_buffer
      - .actual_access:  write_only
        .address_space:  global
        .offset:         96
        .size:           8
        .value_kind:     global_buffer
    .group_segment_fixed_size: 9216
    .kernarg_segment_align: 8
    .kernarg_segment_size: 104
    .language:       OpenCL C
    .language_version:
      - 2
      - 0
    .max_flat_workgroup_size: 512
    .name:           _Z6k_lstmILi256ELi10ELb1ELb0EEvPKDF16_S1_S1_PKfPDF16_S1_S1_S1_S3_S3_S3_PfS5_
    .private_segment_fixed_size: 0
    .sgpr_count:     37
    .sgpr_spill_count: 0
    .symbol:         _Z6k_lstmILi256ELi10ELb1ELb0EEvPKDF16_S1_S1_PKfPDF16_S1_S1_S1_S3_S3_S3_PfS5_.kd
    .uniform_work_group_size: 1
    .uses_dynamic_stack: false
    .vgpr_count:     256
    .vgpr_spill_count: 0
    .wavefront_size: 64
  - .agpr_count:     0
    .args:
      - .actual_access:  read_only
        .address_space:  global
        .offset:         0
        .size:           8
        .value_kind:     global_buffer
      - .actual_access:  read_only
        .address_space:  global
        .offset:         8
        .size:           8
        .value_kind:     global_buffer
      - .actual_access:  read_only
        .address_space:  global
        .offset:         16
        .size:           8
        .value_kind:     global_buffer
      - .actual_access:  read_only
        .address_space:  global
        .offset:         24
        .size:           8
        .value_kind:     global_buffer
      - .actual_access:  read_only
        .address_space:  global
        .offset:         32
        .size:           8
        .value_kind:     global_buffer
      - .actual_access:  read_only
        .address_space:  global
        .offset:         40
        .size:           8
        .value_kind:     global_buffer
      - .actual_access:  read_only
        .address_space:  global
        .offset:         48
        .size:           8
        .value_kind:     global_buffer
      - .actual_access:  read_only
        .address_space:  global
        .offset:         56
        .size:           8
        .value_kind:     global_buffer
      - .actual_access:  read_only
        .address_space:  global
        .offset:         64
        .size:           8
        .value_kind:     global_buffer
      - .actual_access:  read_only
        .address_space:  global
        .offset:         72
        .size:           8
        .value_kind:     global_buffer
      - .actual_access:  read_only
        .address_space:  global
        .offset:         80
        .size:           8
        .value_kind:     global_buffer
      - .actual_access:  write_only
        .address_space:  global
        .offset:         88
        .size:           8
        .value_kind:     global_buffer
      - .actual_access:  read_only
        .address_space:  global
        .offset:         96
        .size:           8
        .value_kind:     global_buffer
    .group_segment_fixed_size: 0
    .kernarg_segment_align: 8
    .kernarg_segment_size: 104
    .language:       OpenCL C
    .language_version:
      - 2
      - 0
    .max_flat_workgroup_size: 512
    .name:           _Z6k_lstmILi128ELi8ELb0ELb1EEvPKDF16_S1_S1_PKfPDF16_S1_S1_S1_S3_S3_S3_PfS5_
    .private_segment_fixed_size: 0
    .sgpr_count:     46
    .sgpr_spill_count: 0
    .symbol:         _Z6k_lstmILi128ELi8ELb0ELb1EEvPKDF16_S1_S1_PKfPDF16_S1_S1_S1_S3_S3_S3_PfS5_.kd
    .uniform_work_group_size: 1
    .uses_dynamic_stack: false
    .vgpr_count:     256
    .vgpr_spill_count: 0
    .wavefront_size: 64
